# baseline (speedup 1.0000x reference)
.LBB3_1:
	s_lshl_b32 s12, s3, 15
	v_or_b32_e32 v67, s12, v65
	s_waitcnt lgkmcnt(0)
	v_mfma_f32_16x16x32_f16 v[54:57], v[22:25], v[10:13], v[54:57]
	ds_read_b128 v[68:71], v67 offset:1024
	ds_read_b128 v[72:75], v67 offset:3072
	v_or_b32_e32 v67, s12, v64
	v_mfma_f32_16x16x32_f16 v[50:53], v[18:21], v[10:13], v[50:53]
	ds_read_b128 v[76:79], v67 offset:17408
	ds_read_b128 v[80:83], v67 offset:19456
	s_add_i32 s3, s3, 1
	v_mfma_f32_16x16x32_f16 v[46:49], v[26:29], v[10:13], v[46:49]
	ds_read_b128 v[84:87], v67 offset:21504
	ds_read_b128 v[88:91], v67 offset:23552
	v_mfma_f32_16x16x32_f16 v[42:45], v[14:17], v[10:13], v[42:45]
	v_mfma_f32_16x16x32_f16 v[38:41], v[22:25], v[6:9], v[38:41]
	v_mfma_f32_16x16x32_f16 v[34:37], v[18:21], v[6:9], v[34:37]
	v_mfma_f32_16x16x32_f16 v[30:33], v[26:29], v[6:9], v[30:33]
	v_mfma_f32_16x16x32_f16 v[2:5], v[14:17], v[6:9], v[2:5]
	v_or_b32_e32 v10, s12, v66
	v_lshl_add_u64 v[6:7], v[60:61], 0, s[4:5]
	v_readfirstlane_b32 s20, v10
	v_lshl_add_u64 v[92:93], v[6:7], 0, s[6:7]
	v_lshl_add_u64 v[94:95], v[6:7], 0, s[10:11]
	v_lshl_add_u64 v[6:7], v[58:59], 0, s[4:5]
	v_lshl_add_u64 v[96:97], v[6:7], 0, s[6:7]
	v_lshl_add_u64 v[98:99], v[6:7], 0, s[10:11]
	s_mov_b32 m0, s20
	s_waitcnt vmcnt(4) lgkmcnt(0)
	s_barrier
	global_load_lds_dwordx4 v[92:93], off
	s_add_u32 m0, s20, 0x2000
	s_nop 0
	global_load_lds_dwordx4 v[94:95], off
	s_add_u32 m0, s20, 0x4000
	s_nop 0
	global_load_lds_dwordx4 v[96:97], off
	s_add_u32 m0, s20, 0x6000
	s_nop 0
	global_load_lds_dwordx4 v[98:99], off
	s_cmp_lg_u32 s3, 3
	s_cselect_b32 s3, s3, 0
	s_lshl_b32 s12, s3, 15
	v_or_b32_e32 v6, s12, v65
	v_or_b32_e32 v14, s12, v64
	s_waitcnt lgkmcnt(0)
	v_mfma_f32_16x16x32_f16 v[54:57], v[76:79], v[68:71], v[54:57]
	ds_read_b128 v[10:13], v6
	ds_read_b128 v[6:9], v6 offset:2048
	v_mfma_f32_16x16x32_f16 v[50:53], v[80:83], v[68:71], v[50:53]
	ds_read_b128 v[22:25], v14 offset:16384
	ds_read_b128 v[18:21], v14 offset:18432
	v_mfma_f32_16x16x32_f16 v[46:49], v[84:87], v[68:71], v[46:49]
	ds_read_b128 v[26:29], v14 offset:20480
	ds_read_b128 v[14:17], v14 offset:22528
	v_mfma_f32_16x16x32_f16 v[42:45], v[88:91], v[68:71], v[42:45]
	v_mfma_f32_16x16x32_f16 v[38:41], v[76:79], v[72:75], v[38:41]
	v_mfma_f32_16x16x32_f16 v[34:37], v[80:83], v[72:75], v[34:37]
	v_mfma_f32_16x16x32_f16 v[30:33], v[84:87], v[72:75], v[30:33]
	v_mfma_f32_16x16x32_f16 v[2:5], v[88:91], v[72:75], v[2:5]
	s_add_u32 s4, s4, 0x80
	s_addc_u32 s5, s5, 0
	s_cmpk_eq_i32 s4, 0x680
	s_cbranch_scc0 .LBB3_1
	s_waitcnt lgkmcnt(0)
	v_mfma_f32_16x16x32_f16 v[54:57], v[22:25], v[10:13], v[54:57]
	ds_read_b128 v[58:61], v65 offset:33792
	ds_read_b128 v[66:69], v65 offset:35840
	v_mfma_f32_16x16x32_f16 v[50:53], v[18:21], v[10:13], v[50:53]
	ds_read_b128 v[70:73], v64 offset:50176
	ds_read_b128 v[74:77], v64 offset:52224
	v_mfma_f32_16x16x32_f16 v[46:49], v[26:29], v[10:13], v[46:49]
	ds_read_b128 v[78:81], v64 offset:54272
	ds_read_b128 v[82:85], v64 offset:56320
	v_mfma_f32_16x16x32_f16 v[10:13], v[14:17], v[10:13], v[42:45]
	v_mfma_f32_16x16x32_f16 v[22:25], v[22:25], v[6:9], v[38:41]
	v_mfma_f32_16x16x32_f16 v[18:21], v[18:21], v[6:9], v[34:37]
	v_mfma_f32_16x16x32_f16 v[26:29], v[26:29], v[6:9], v[30:33]
	v_mfma_f32_16x16x32_f16 v[2:5], v[14:17], v[6:9], v[2:5]
	v_or_b32_e32 v14, 0x10000, v65
	s_nop 0
	v_add_u32_e32 v30, 0x10800, v65
	s_waitcnt vmcnt(4) lgkmcnt(0)
	s_barrier
	s_waitcnt lgkmcnt(0)
	v_mfma_f32_16x16x32_f16 v[6:9], v[70:73], v[58:61], v[54:57]
	ds_read_b128 v[14:17], v14
	ds_read_b128 v[30:33], v30
	v_or_b32_e32 v38, 0x14000, v64
	v_mfma_f32_16x16x32_f16 v[34:37], v[74:77], v[58:61], v[50:53]
	v_add_u32_e32 v42, 0x14800, v64
	v_add_u32_e32 v54, 0x15800, v64
	ds_read_b128 v[38:41], v38
	v_add_u32_e32 v50, 0x15000, v64
	ds_read_b128 v[42:45], v42
	v_mfma_f32_16x16x32_f16 v[46:49], v[78:81], v[58:61], v[46:49]
	ds_read_b128 v[50:53], v50
	ds_read_b128 v[54:57], v54
	v_mfma_f32_16x16x32_f16 v[10:13], v[82:85], v[58:61], v[10:13]
	v_mfma_f32_16x16x32_f16 v[22:25], v[70:73], v[66:69], v[22:25]
	v_mfma_f32_16x16x32_f16 v[18:21], v[74:77], v[66:69], v[18:21]
	v_mfma_f32_16x16x32_f16 v[26:29], v[78:81], v[66:69], v[26:29]
	v_mfma_f32_16x16x32_f16 v[2:5], v[82:85], v[66:69], v[2:5]
	v_add_u32_e32 v58, 0x10400, v65
	v_add_u32_e32 v66, 0x10c00, v65
	v_add_u32_e32 v70, 0x14400, v64
	v_add_u32_e32 v74, 0x14c00, v64
	v_add_u32_e32 v78, 0x15400, v64
	v_add_u32_e32 v82, 0x15c00, v64
	s_waitcnt lgkmcnt(0)
	v_mfma_f32_16x16x32_f16 v[6:9], v[38:41], v[14:17], v[6:9]
	ds_read_b128 v[58:61], v58
	ds_read_b128 v[66:69], v66
	v_mfma_f32_16x16x32_f16 v[34:37], v[42:45], v[14:17], v[34:37]
	ds_read_b128 v[70:73], v70
	ds_read_b128 v[74:77], v74
	v_mfma_f32_16x16x32_f16 v[46:49], v[50:53], v[14:17], v[46:49]
	ds_read_b128 v[78:81], v78
	ds_read_b128 v[82:85], v82
	v_mfma_f32_16x16x32_f16 v[10:13], v[54:57], v[14:17], v[10:13]
	v_mfma_f32_16x16x32_f16 v[14:17], v[38:41], v[30:33], v[22:25]
	v_mfma_f32_16x16x32_f16 v[18:21], v[42:45], v[30:33], v[18:21]
	v_mfma_f32_16x16x32_f16 v[22:25], v[50:53], v[30:33], v[26:29]
	v_mfma_f32_16x16x32_f16 v[2:5], v[54:57], v[30:33], v[2:5]
	s_waitcnt vmcnt(0) lgkmcnt(0)
	s_waitcnt lgkmcnt(0)
	v_mfma_f32_16x16x32_f16 v[6:9], v[70:73], v[58:61], v[6:9]
	s_barrier
	ds_read_b128 v[26:29], v65
	ds_read_b128 v[30:33], v65 offset:2048
	v_mfma_f32_16x16x32_f16 v[34:37], v[74:77], v[58:61], v[34:37]
	ds_read_b128 v[38:41], v64 offset:16384
	ds_read_b128 v[42:45], v64 offset:18432
	v_mfma_f32_16x16x32_f16 v[46:49], v[78:81], v[58:61], v[46:49]
	ds_read_b128 v[50:53], v64 offset:20480
	ds_read_b128 v[54:57], v64 offset:22528
	v_mfma_f32_16x16x32_f16 v[10:13], v[82:85], v[58:61], v[10:13]
	v_mfma_f32_16x16x32_f16 v[14:17], v[70:73], v[66:69], v[14:17]
	v_mfma_f32_16x16x32_f16 v[18:21], v[74:77], v[66:69], v[18:21]
	v_mfma_f32_16x16x32_f16 v[22:25], v[78:81], v[66:69], v[22:25]
	v_mfma_f32_16x16x32_f16 v[2:5], v[82:85], v[66:69], v[2:5]
	s_waitcnt lgkmcnt(0)
	v_mfma_f32_16x16x32_f16 v[6:9], v[38:41], v[26:29], v[6:9]
	ds_read_b128 v[58:61], v64 offset:19456
	s_lshl_b64 s[0:1], s[0:1], 2
	v_lshl_add_u32 v63, v63, 5, s2
	v_mfma_f32_16x16x32_f16 v[34:37], v[42:45], v[26:29], v[34:37]
	s_add_u32 s0, s8, s0
	v_and_or_b32 v0, v0, 15, v63
	s_addc_u32 s1, s9, s1
	v_mfma_f32_16x16x32_f16 v[46:49], v[50:53], v[26:29], v[46:49]
	v_and_b32_e32 v1, 12, v1
	v_mfma_f32_16x16x32_f16 v[10:13], v[54:57], v[26:29], v[10:13]
	ds_read_b128 v[26:29], v65 offset:1024
	v_mfma_f32_16x16x32_f16 v[14:17], v[38:41], v[30:33], v[14:17]
	ds_read_b128 v[38:41], v65 offset:3072
	v_mfma_f32_16x16x32_f16 v[18:21], v[42:45], v[30:33], v[18:21]
	ds_read_b128 v[42:45], v64 offset:17408
	v_mfma_f32_16x16x32_f16 v[22:25], v[50:53], v[30:33], v[22:25]
	ds_read_b128 v[50:53], v64 offset:21504
	ds_read_b128 v[64:67], v64 offset:23552
	v_mfma_f32_16x16x32_f16 v[2:5], v[54:57], v[30:33], v[2:5]
	v_lshlrev_b32_e32 v54, 8, v62
	v_mov_b32_e32 v55, 0
	v_lshl_add_u64 v[56:57], s[0:1], 0, v[54:55]
	s_waitcnt lgkmcnt(0)
	v_mfma_f32_16x16x32_f16 v[6:9], v[42:45], v[26:29], v[6:9]
	v_lshlrev_b32_e32 v54, 2, v1
	v_ashrrev_i32_e32 v1, 31, v0
	v_mfma_f32_16x16x32_f16 v[10:13], v[64:67], v[26:29], v[10:13]
	v_mfma_f32_16x16x32_f16 v[30:33], v[58:61], v[26:29], v[34:37]
	v_mfma_f32_16x16x32_f16 v[34:37], v[50:53], v[26:29], v[46:49]
	s_nop 2
	v_lshlrev_b64 v[48:49], 12, v[0:1]
	v_or_b32_e32 v0, 16, v0
	v_lshl_add_u64 v[46:47], v[56:57], 0, v[54:55]
	v_ashrrev_i32_e32 v1, 31, v0
	v_lshl_add_u64 v[26:27], v[46:47], 0, v[48:49]
	v_lshlrev_b64 v[0:1], 12, v[0:1]
	global_store_dwordx4 v[26:27], v[6:9], off sc1
	global_store_dwordx4 v[26:27], v[10:13], off offset:192 sc1
	global_store_dwordx4 v[26:27], v[30:33], off offset:64 sc1
	v_mfma_f32_16x16x32_f16 v[6:9], v[42:45], v[38:41], v[14:17]
	global_store_dwordx4 v[26:27], v[34:37], off offset:128 sc1
	v_mfma_f32_16x16x32_f16 v[10:13], v[58:61], v[38:41], v[18:21]
	s_nop 2
	v_lshl_add_u64 v[18:19], v[46:47], 0, v[0:1]
	v_mfma_f32_16x16x32_f16 v[14:17], v[50:53], v[38:41], v[22:25]
	s_nop 0
	global_store_dwordx4 v[18:19], v[6:9], off sc1
	s_nop 0
	global_store_dwordx4 v[18:19], v[10:13], off offset:64 sc1
	v_mfma_f32_16x16x32_f16 v[0:3], v[64:67], v[38:41], v[2:5]
	s_nop 2
	global_store_dwordx4 v[18:19], v[14:17], off offset:128 sc1
	s_nop 3
	global_store_dwordx4 v[18:19], v[0:3], off offset:192 sc1
	s_endpgm

	.amdhsa_kernel _Z9gemm_gldsILi128ELi128ELi4ELi2ELi3ELi8ELi4ELi1ELi4096ELi1024ELi1024EEvPKDF16_S1_PfPKfS4_PKiPDF16_S7_S7_
		.amdhsa_group_segment_fixed_size 98304
		.amdhsa_private_segment_fixed_size 0
		.amdhsa_kernarg_size 72
		.amdhsa_user_sgpr_count 2
		.amdhsa_user_sgpr_dispatch_ptr 0
		.amdhsa_user_sgpr_queue_ptr 0
		.amdhsa_user_sgpr_kernarg_segment_ptr 1
		.amdhsa_user_sgpr_dispatch_id 0
		.amdhsa_user_sgpr_kernarg_preload_length 0
		.amdhsa_user_sgpr_kernarg_preload_offset 0
		.amdhsa_user_sgpr_private_segment_size 0
		.amdhsa_uses_dynamic_stack 0
		.amdhsa_enable_private_segment 0
		.amdhsa_system_sgpr_workgroup_id_x 1
		.amdhsa_system_sgpr_workgroup_id_y 0
		.amdhsa_system_sgpr_workgroup_id_z 0
		.amdhsa_system_sgpr_workgroup_info 0
		.amdhsa_system_vgpr_workitem_id 0
		.amdhsa_next_free_vgpr 169
		.amdhsa_next_free_sgpr 96
		.amdhsa_accum_offset 100
		.amdhsa_reserve_vcc 0
		.amdhsa_float_round_mode_32 0
		.amdhsa_float_round_mode_16_64 0
		.amdhsa_float_denorm_mode_32 3
		.amdhsa_float_denorm_mode_16_64 3
		.amdhsa_dx10_clamp 1
		.amdhsa_ieee_mode 1
		.amdhsa_fp16_overflow 0
		.amdhsa_tg_split 0
		.amdhsa_exception_fp_ieee_invalid_op 0
		.amdhsa_exception_fp_denorm_src 0
		.amdhsa_exception_fp_ieee_div_zero 0
		.amdhsa_exception_fp_ieee_overflow 0
		.amdhsa_exception_fp_ieee_underflow 0
		.amdhsa_exception_fp_ieee_inexact 0
		.amdhsa_exception_int_div_zero 0
	.end_amdhsa_kernel

amdhsa.kernels:
  - .agpr_count:     0
    .args:
      - .actual_access:  read_only
        .address_space:  global
        .offset:         0
        .size:           8
        .value_kind:     global_buffer
      - .actual_access:  read_only
        .address_space:  global
        .offset:         8
        .size:           8
        .value_kind:     global_buffer
      - .actual_access:  read_only
        .address_space:  global
        .offset:         16
        .size:           8
        .value_kind:     global_buffer
      - .actual_access:  read_only
        .address_space:  global
        .offset:         24
        .size:           8
        .value_kind:     global_buffer
      - .actual_access:  read_only
        .address_space:  global
        .offset:         32
        .size:           8
        .value_kind:     global_buffer
      - .actual_access:  read_only
        .address_space:  global
        .offset:         40
        .size:           8
        .value_kind:     global_buffer
      - .actual_access:  write_only
        .address_space:  global
        .offset:         48
        .size:           8
        .value_kind:     global_buffer
      - .actual_access:  write_only
        .address_space:  global
        .offset:         56
        .size:           8
        .value_kind:     global_buffer
      - .actual_access:  write_only
        .address_space:  global
        .offset:         64
        .size:           8
        .value_kind:     global_buffer
      - .actual_access:  write_only
        .address_space:  global
        .offset:         72
        .size:           8
        .value_kind:     global_buffer
      - .actual_access:  write_only
        .address_space:  global
        .offset:         80
        .size:           8
        .value_kind:     global_buffer
    .group_segment_fixed_size: 16640
    .kernarg_segment_align: 8
    .kernarg_segment_size: 88
    .language:       OpenCL C
    .language_version:
      - 2
      - 0
    .max_flat_workgroup_size: 256
    .name:           _Z11prep_kernelPKfS0_S0_S0_S0_PKiPDF16_S3_S3_PyPi
    .private_segment_fixed_size: 0
    .sgpr_count:     54
    .sgpr_spill_count: 0
    .symbol:         _Z11prep_kernelPKfS0_S0_S0_S0_PKiPDF16_S3_S3_PyPi.kd
    .uniform_work_group_size: 1
    .uses_dynamic_stack: false
    .vgpr_count:     46
    .vgpr_spill_count: 0
    .wavefront_size: 64
  - .agpr_count:     0
    .args:
      - .actual_access:  read_only
        .address_space:  global
        .offset:         0
        .size:           8
        .value_kind:     global_buffer
      - .actual_access:  read_only
        .address_space:  global
        .offset:         8
        .size:           8
        .value_kind:     global_buffer
      - .actual_access:  read_only
        .address_space:  global
        .offset:         16
        .size:           8
        .value_kind:     global_buffer
      - .actual_access:  read_only
        .address_space:  global
        .offset:         24
        .size:           8
        .value_kind:     global_buffer
      - .actual_access:  read_only
        .address_space:  global
        .offset:         32
        .size:           8
        .value_kind:     global_buffer
      - .actual_access:  write_only
        .address_space:  global
        .offset:         40
        .size:           8
        .value_kind:     global_buffer
    .group_segment_fixed_size: 36864
    .kernarg_segment_align: 8
    .kernarg_segment_size: 48
    .language:       OpenCL C
    .language_version:
      - 2
      - 0
    .max_flat_workgroup_size: 256
    .name:           _Z11attn_kernelPKDF16_S0_S0_PKyPKiPDF16_
    .private_segment_fixed_size: 0
    .sgpr_count:     32
    .sgpr_spill_count: 0
    .symbol:         _Z11attn_kernelPKDF16_S0_S0_PKyPKiPDF16_.kd
    .uniform_work_group_size: 1
    .uses_dynamic_stack: false
    .vgpr_count:     124
    .vgpr_spill_count: 0
    .wavefront_size: 64
  - .agpr_count:     0
    .args:
      - .address_space:  global
        .offset:         0
        .size:           8
        .value_kind:     global_buffer
      - .address_space:  global
        .offset:         8
        .size:           8
        .value_kind:     global_buffer
      - .actual_access:  read_only
        .address_space:  global
        .offset:         16
        .size:           8
        .value_kind:     global_buffer
      - .actual_access:  read_only
        .address_space:  global
        .offset:         24
        .size:           8
        .value_kind:     global_buffer
      - .actual_access:  read_only
        .address_space:  global
        .offset:         32
        .size:           8
        .value_kind:     global_buffer
      - .actual_access:  read_only
        .address_space:  global
        .offset:         40
        .size:           8
        .value_kind:     global_buffer
      - .actual_access:  write_only
        .address_space:  global
        .offset:         48
        .size:           8
        .value_kind:     global_buffer
      - .actual_access:  write_only
        .address_space:  global
        .offset:         56
        .size:           8
        .value_kind:     global_buffer
      - .actual_access:  write_only
        .address_space:  global
        .offset:         64
        .size:           8
        .value_kind:     global_buffer
    .group_segment_fixed_size: 114688
    .kernarg_segment_align: 8
    .kernarg_segment_size: 72
    .language:       OpenCL C
    .language_version:
      - 2
      - 0
    .max_flat_workgroup_size: 512
    .name:           _Z9gemm_gldsILi256ELi192ELi4ELi2ELi2ELi4ELi8ELi0ELi4096ELi3072ELi1024EEvPKDF16_S1_PfPKfS4_PKiPDF16_S7_S7_
    .private_segment_fixed_size: 0
    .sgpr_count:     29
    .sgpr_spill_count: 0
    .symbol:         _Z9gemm_gldsILi256ELi192ELi4ELi2ELi2ELi4ELi8ELi0ELi4096ELi3072ELi1024EEvPKDF16_S1_PfPKfS4_PKiPDF16_S7_S7_.kd
    .uniform_work_group_size: 1
    .uses_dynamic_stack: false
    .vgpr_count:     217
    .vgpr_spill_count: 0
    .wavefront_size: 64
  - .agpr_count:     0
    .args:
      - .address_space:  global
        .offset:         0
        .size:           8
        .value_kind:     global_buffer
      - .address_space:  global
        .offset:         8
        .size:           8
        .value_kind:     global_buffer
      - .actual_access:  write_only
        .address_space:  global
        .offset:         16
        .size:           8
        .value_kind:     global_buffer
      - .actual_access:  read_only
        .address_space:  global
        .offset:         24
        .size:           8
        .value_kind:     global_buffer
      - .actual_access:  read_only
        .address_space:  global
        .offset:         32
        .size:           8
        .value_kind:     global_buffer
      - .actual_access:  read_only
        .address_space:  global
        .offset:         40
        .size:           8
        .value_kind:     global_buffer
      - .actual_access:  read_only
        .address_space:  global
        .offset:         48
        .size:           8
        .value_kind:     global_buffer
      - .actual_access:  read_only
        .address_space:  global
        .offset:         56
        .size:           8
        .value_kind:     global_buffer
      - .actual_access:  read_only
        .address_space:  global
        .offset:         64
        .size:           8
        .value_kind:     global_buffer
    .group_segment_fixed_size: 98304
    .kernarg_segment_align: 8
    .kernarg_segment_size: 72
    .language:       OpenCL C
    .language_version:
      - 2
      - 0
    .max_flat_workgroup_size: 512
    .name:           _Z9gemm_gldsILi128ELi128ELi4ELi2ELi3ELi8ELi4ELi1ELi4096ELi1024ELi1024EEvPKDF16_S1_PfPKfS4_PKiPDF16_S7_S7_
    .private_segment_fixed_size: 0
    .sgpr_count:     20
    .sgpr_spill_count: 0
    .symbol:         _Z9gemm_gldsILi128ELi128ELi4ELi2ELi3ELi8ELi4ELi1ELi4096ELi1024ELi1024EEvPKDF16_S1_PfPKfS4_PKiPDF16_S7_S7_.kd
    .uniform_work_group_size: 1
    .uses_dynamic_stack: false
    .vgpr_count:     100
    .vgpr_spill_count: 0
    .wavefront_size: 64
